# strategy: hide load latency behind independent setup - M1 per-unit gather-index wait moved ~55 instructions later, right before the first use
# speedup vs baseline: 1.0046x; 1.0009x over previous
;     ...
;             if constexpr (GATHER) { if (last && has_next) {
; #pragma unroll
;                 for (int h = 0; h < 2; ++h)
; #pragma unroll
;                     for (int i = 0; i < 2; ++i) { int _R, _C; stage_rc(tid * 16 + i * 8192, _R, _C); gc[h][i] = gn[h][i] * (unsigned)(lda * 2) + (unsigned)(_C * 2); } } }
;     ...
; #pragma unroll
;         for (int a = 0; a < 2; ++a)
; #pragma unroll
;             for (int b = 0; b < 2; ++b)
; #pragma unroll
;                 for (int m = 0; m < 4; ++m)
; #pragma unroll
;                     for (int n = 0; n < 2; ++n) acc[a][b][m][n] = (f32x4){0.f, 0.f, 0.f, 0.f};
.LBB0_1215:
	s_and_b64 s[22:23], s[26:27], exec
	s_cselect_b32 s17, s11, s11
	s_cselect_b32 s25, s10, s10
	s_cselect_b32 s48, s21, s9
	s_cselect_b32 s49, s20, s8
	s_ashr_i32 s3, s2, 31
	s_lshl_b64 s[30:31], s[2:3], 13
	s_lshl_b32 s2, s6, 7
	s_ashr_i32 s3, s2, 31
	s_cmp_lg_u32 s0, 2
	s_cselect_b64 s[28:29], -1, 0
	s_cmp_lg_u32 s0, 1
	s_cselect_b64 s[22:23], -1, 0
	s_add_u32 s6, s45, s30
	s_addc_u32 s7, s41, s31
	s_lshl_b64 s[0:1], s[2:3], 2
	s_add_u32 s30, s6, s0
	s_addc_u32 s31, s7, s1
	s_waitcnt lgkmcnt(0)
	v_mov_b32_e32 v2, v1
	v_mov_b32_e32 v3, v1
	s_add_u32 s0, s8, 0x100
	v_mov_b32_e32 v0, v1
	v_mov_b64_e32 v[68:69], v[2:3]
	v_mov_b64_e32 v[72:73], v[2:3]
	v_mov_b64_e32 v[84:85], v[2:3]
	v_mov_b64_e32 v[88:89], v[2:3]
	v_mov_b64_e32 v[100:101], v[2:3]
	v_mov_b64_e32 v[104:105], v[2:3]
	v_mov_b64_e32 v[116:117], v[2:3]
	v_mov_b64_e32 v[120:121], v[2:3]
	v_mov_b64_e32 v[76:77], v[2:3]
	v_mov_b64_e32 v[80:81], v[2:3]
	v_mov_b64_e32 v[92:93], v[2:3]
	v_mov_b64_e32 v[96:97], v[2:3]
	v_mov_b64_e32 v[108:109], v[2:3]
	v_mov_b64_e32 v[112:113], v[2:3]
	v_mov_b64_e32 v[124:125], v[2:3]
	v_mov_b64_e32 v[128:129], v[2:3]
	v_mov_b64_e32 v[132:133], v[2:3]
	v_mov_b64_e32 v[136:137], v[2:3]
	v_mov_b64_e32 v[148:149], v[2:3]
	v_mov_b64_e32 v[152:153], v[2:3]
	v_mov_b64_e32 v[164:165], v[2:3]
	v_mov_b64_e32 v[168:169], v[2:3]
	v_mov_b64_e32 v[180:181], v[2:3]
	v_mov_b64_e32 v[184:185], v[2:3]
	v_mov_b64_e32 v[140:141], v[2:3]
	v_mov_b64_e32 v[144:145], v[2:3]
	v_mov_b64_e32 v[156:157], v[2:3]
	v_mov_b64_e32 v[160:161], v[2:3]
	v_mov_b64_e32 v[172:173], v[2:3]
	v_mov_b64_e32 v[176:177], v[2:3]
	v_mov_b64_e32 v[188:189], v[2:3]
	v_mov_b64_e32 v[192:193], v[2:3]
	s_waitcnt vmcnt(0)
	v_ashrrev_i32_e32 v226, 2, v226
	v_ashrrev_i32_e32 v225, 2, v225
	v_ashrrev_i32_e32 v228, 2, v228
	v_ashrrev_i32_e32 v227, 2, v227
	v_lshl_add_u32 v229, v226, 10, v216
	v_lshl_add_u32 v230, v225, 10, v219
	v_lshl_add_u32 v231, v228, 10, v216
	v_lshl_add_u32 v232, v227, 10, v219
	s_addc_u32 s1, s9, 0
	s_mov_b32 s3, -2
	s_mov_b64 s[34:35], 0
	v_mov_b64_e32 v[66:67], v[0:1]
	v_mov_b64_e32 v[70:71], v[0:1]
	v_mov_b64_e32 v[82:83], v[0:1]
	v_mov_b64_e32 v[86:87], v[0:1]
	v_mov_b64_e32 v[98:99], v[0:1]
	v_mov_b64_e32 v[102:103], v[0:1]
	v_mov_b64_e32 v[114:115], v[0:1]
	v_mov_b64_e32 v[118:119], v[0:1]
	v_mov_b64_e32 v[74:75], v[0:1]
	v_mov_b64_e32 v[78:79], v[0:1]
	v_mov_b64_e32 v[90:91], v[0:1]
	v_mov_b64_e32 v[94:95], v[0:1]
	v_mov_b64_e32 v[106:107], v[0:1]
	v_mov_b64_e32 v[110:111], v[0:1]
	v_mov_b64_e32 v[122:123], v[0:1]
	v_mov_b64_e32 v[126:127], v[0:1]
	v_mov_b64_e32 v[130:131], v[0:1]
	v_mov_b64_e32 v[134:135], v[0:1]
	v_mov_b64_e32 v[146:147], v[0:1]
	v_mov_b64_e32 v[150:151], v[0:1]
	v_mov_b64_e32 v[162:163], v[0:1]
	v_mov_b64_e32 v[166:167], v[0:1]
	v_mov_b64_e32 v[178:179], v[0:1]
	v_mov_b64_e32 v[182:183], v[0:1]
	v_mov_b64_e32 v[138:139], v[0:1]
	v_mov_b64_e32 v[142:143], v[0:1]
	v_mov_b64_e32 v[154:155], v[0:1]
	v_mov_b64_e32 v[158:159], v[0:1]
	v_mov_b64_e32 v[170:171], v[0:1]
	v_mov_b64_e32 v[174:175], v[0:1]
	v_mov_b64_e32 v[186:187], v[0:1]
	v_mov_b64_e32 v[190:191], v[0:1]
	s_branch .LBB0_1217
